# speedup vs baseline: 1.0055x; 1.0055x over previous
.LBB1_235:
	v_add_u32_e32 v0, s66, v0
	v_subrev_u32_e32 v0, 0x100, v0
	s_movk_i32 s0, 0xf0
	v_cmp_gt_u32_e32 vcc, s0, v0
	s_and_saveexec_b64 s[0:1], vcc
	s_cbranch_execz .Lepi_idle
	s_load_dwordx4 s[68:71], s[14:15], 0x0
	s_load_dwordx2 s[72:73], s[14:15], 0x10
	s_movk_i32 s0, 0x77
	v_mov_b32_e32 v1, 0xffffff88
	v_cmp_lt_u32_e32 vcc, s0, v0
	v_mov_b32_e32 v2, 0x44704000
	s_mov_b32 s0, 0xf800000
	v_cndmask_b32_e32 v1, 0, v1, vcc
	v_add_u32_e32 v0, v1, v0
	v_cvt_f32_u32_e32 v1, v0
	s_mov_b32 s5, 0x17800
	s_mov_b32 s4, 0x3eb17218
	v_fmac_f32_e32 v2, 0xc1000000, v1
	v_sqrt_f32_e32 v1, v2
	s_nop 0
	v_sub_f32_e32 v1, 0x41f80000, v1
	v_mul_f32_e32 v1, 0.5, v1
	v_cvt_i32_f32_e32 v1, v1
	s_and_b64 s[0:1], exec, s[16:17]
	s_cselect_b32 s2, s40, s38
	s_cselect_b32 s3, s39, s33
	v_sub_u32_e32 v2, 31, v1
	v_mul_u32_u24_e32 v2, v2, v1
	v_lshrrev_b32_e32 v3, 31, v2
	v_add_u32_e32 v2, v2, v3
	v_ashrrev_i32_e32 v2, 1, v2
	v_cmp_gt_i32_e64 s[0:1], v2, v0
	s_nop 1
	v_subbrev_co_u32_e64 v1, s[0:1], 0, v1, s[0:1]
	v_add_u32_e32 v2, 1, v1
	v_sub_u32_e32 v3, 30, v1
	v_mul_u32_u24_e32 v3, v2, v3
	v_lshrrev_b32_e32 v4, 31, v3
	v_add_u32_e32 v3, v3, v4
	v_ashrrev_i32_e32 v3, 1, v3
	v_cmp_gt_i32_e64 s[0:1], v3, v0
	s_nop 1
	v_cndmask_b32_e64 v12, v2, v1, s[0:1]
	v_sub_u32_e32 v1, 31, v12
	v_mul_u32_u24_e32 v1, v1, v12
	v_lshrrev_b32_e32 v2, 31, v1
	v_add_u32_e32 v1, v1, v2
	v_ashrrev_i32_e32 v1, 1, v1
	v_sub_u32_e32 v0, v0, v1
	v_cndmask_b32_e64 v1, 0, 16, vcc
	v_lshl_or_b32 v1, s2, 5, v1
	v_add_u32_e32 v1, v1, v12
	v_sub_u32_e32 v2, 0xff, v1
	v_mul_u32_u24_e32 v1, v2, v1
	v_lshrrev_b32_e32 v2, 31, v1
	v_add_u32_e32 v1, v1, v2
	v_ashrrev_i32_e32 v1, 1, v1
	v_add3_u32 v13, v12, v0, 1
	v_add_u32_e32 v0, v1, v0
	v_ashrrev_i32_e32 v1, 31, v0
	v_mov_b32_e32 v2, 0x1fc0
	v_mad_u64_u32 v[0:1], s[0:1], s3, v2, v[0:1]
	v_mad_u64_u32 v[4:5], s[0:1], v0, 24, s[10:11]
	v_mad_i32_i24 v5, v1, 24, v5
	v_mov_b32_e32 v0, 0x17800
	v_lshl_add_u32 v14, v12, 2, v0
	v_mov_b32_e32 v0, 0x60
	v_cndmask_b32_e32 v15, 0, v0, vcc
	v_lshlrev_b32_e32 v16, 2, v13
	v_add_lshl_u32 v0, v15, v12, 6
	v_add3_u32 v16, v0, v16, s5
	v_add_u32_e32 v1, v15, v13
	v_lshl_add_u32 v17, v1, 6, v14
	ds_read_b32 v0, v16
	ds_read_b32 v2, v17
	ds_read_b32 v1, v16 offset:1024
	ds_read_b32 v3, v17 offset:1024
	ds_read_b32 v6, v16 offset:2048
	ds_read_b32 v8, v17 offset:2048
	ds_read_b32 v7, v16 offset:3072
	ds_read_b32 v9, v17 offset:3072
	ds_read_b32 v12, v16 offset:4096
	ds_read_b32 v14, v17 offset:4096
	ds_read_b32 v13, v16 offset:5120
	ds_read_b32 v15, v17 offset:5120
	s_waitcnt lgkmcnt(0)
	v_pk_add_f32 v[0:1], v[0:1], v[2:3]
	v_mov_b32_e32 v2, s70
	v_mov_b32_e32 v3, s71
	v_mov_b64_e32 v[10:11], s[68:69]
	v_pk_add_f32 v[6:7], v[6:7], v[8:9]
	v_pk_fma_f32 v[0:1], v[0:1], s[4:5], v[10:11] op_sel_hi:[1,0,1]
	v_pk_fma_f32 v[2:3], v[6:7], s[4:5], v[2:3] op_sel_hi:[1,0,1]
	global_store_dwordx4 v[4:5], v[0:3], off
	s_nop 1
	v_pk_add_f32 v[0:1], v[12:13], v[14:15]
	v_mov_b64_e32 v[2:3], s[72:73]
	v_pk_fma_f32 v[0:1], v[0:1], s[4:5], v[2:3] op_sel_hi:[1,0,1]
	global_store_dwordx2 v[4:5], v[0:1], off offset:16
	s_endpgm
